# in-projection GEMM non-RoPE epilogue: v_permlane16_swap pairs the n=0/n=1 pieces across 16-lane rows so each lane stores 16 contiguous bytes (dwordx4, half the store instructions); on top of P5/P7 wai
# baseline (speedup 1.0000x reference)
; __device__ __forceinline__ v2u pk4(f32x4 v) { v2u r; r.x = pk2(v.x, v.y); r.y = pk2(v.z, v.w); return r; }
;     __device__ __forceinline__ void operator()(const pg8::f32x4 (&acc)[2][2][4][2], const pg8::Unit& u, int wr, int wc, int fr, int fq) const {
;     ...
; #pragma unroll
;             for (int ai = 0; ai < 2; ++ai)
; #pragma unroll
;                 for (int m = 0; m < 4; ++m) {
;                     const int row = u.pm * 256 + ai * 128 + wr * 64 + m * 16 + fr;
;                     bf16* rp = base + (size_t)row * ld + cb + 32 * wc + 4 * fq;
; #pragma unroll
;                     for (int bj = 0; bj < 2; ++bj)
; #pragma unroll
;                         for (int n = 0; n < 2; ++n) *(v2u*)(rp + 128 * bj + 16 * n) = pk4(acc[ai][bj][m][n]);
;                 }
.LBB0_339:
	v_bfe_u32 v142, v0, 4, 1
	v_mul_u32_u24_e32 v142, 24, v142
	v_mov_b32_e32 v143, 0
	s_lshl_b64 s[62:63], s[10:11], 1
	s_add_u32 s9, s96, s62
	s_addc_u32 s10, s97, s63
	s_add_u32 s62, s9, s17
	s_addc_u32 s63, s10, 0
	s_lshl_b32 s9, s78, 8
	v_mov_b32_e32 v167, v151
	v_add_u32_e32 v132, s9, v153
	v_lshl_add_u64 v[130:131], s[62:63], 0, v[166:167]
	v_mad_i64_i32 v[132:133], s[62:63], s94, v132, 0
	v_lshl_add_u64 v[132:133], v[132:133], 1, v[130:131]
	v_lshl_add_u64 v[144:145], v[132:133], 0, v[142:143]
	v_cvt_pk_bf16_f32 v134, v126, v127
	v_cvt_pk_bf16_f32 v135, v128, v129
	v_cvt_pk_bf16_f32 v136, v122, v123
	v_cvt_pk_bf16_f32 v137, v124, v125
	v_cvt_pk_bf16_f32 v138, v118, v119
	v_cvt_pk_bf16_f32 v139, v120, v121
	v_cvt_pk_bf16_f32 v140, v114, v115
	v_cvt_pk_bf16_f32 v141, v116, v117
	s_nop 1
	v_permlane16_swap_b32_e32 v134, v136
	v_permlane16_swap_b32_e32 v135, v137
	v_permlane16_swap_b32_e32 v138, v140
	v_permlane16_swap_b32_e32 v139, v141
	global_store_dwordx4 v[144:145], v[134:137], off
	global_store_dwordx4 v[144:145], v[138:141], off offset:256
	v_add_u32_e32 v132, s9, v176
	v_mad_i64_i32 v[132:133], s[62:63], s94, v132, 0
	v_lshl_add_u64 v[132:133], v[132:133], 1, v[130:131]
	v_lshl_add_u64 v[144:145], v[132:133], 0, v[142:143]
	v_cvt_pk_bf16_f32 v134, v110, v111
	v_cvt_pk_bf16_f32 v135, v112, v113
	v_cvt_pk_bf16_f32 v136, v106, v107
	v_cvt_pk_bf16_f32 v137, v108, v109
	v_cvt_pk_bf16_f32 v138, v102, v103
	v_cvt_pk_bf16_f32 v139, v104, v105
	v_cvt_pk_bf16_f32 v140, v98, v99
	v_cvt_pk_bf16_f32 v141, v100, v101
	s_nop 1
	v_permlane16_swap_b32_e32 v134, v136
	v_permlane16_swap_b32_e32 v135, v137
	v_permlane16_swap_b32_e32 v138, v140
	v_permlane16_swap_b32_e32 v139, v141
	global_store_dwordx4 v[144:145], v[134:137], off
	global_store_dwordx4 v[144:145], v[138:141], off offset:256
	v_add_u32_e32 v132, s9, v177
	v_mad_i64_i32 v[132:133], s[62:63], s94, v132, 0
	v_lshl_add_u64 v[132:133], v[132:133], 1, v[130:131]
	v_lshl_add_u64 v[144:145], v[132:133], 0, v[142:143]
	v_cvt_pk_bf16_f32 v134, v94, v95
	v_cvt_pk_bf16_f32 v135, v96, v97
	v_cvt_pk_bf16_f32 v136, v90, v91
	v_cvt_pk_bf16_f32 v137, v92, v93
	v_cvt_pk_bf16_f32 v138, v86, v87
	v_cvt_pk_bf16_f32 v139, v88, v89
	v_cvt_pk_bf16_f32 v140, v82, v83
	v_cvt_pk_bf16_f32 v141, v84, v85
	s_nop 1
	v_permlane16_swap_b32_e32 v134, v136
	v_permlane16_swap_b32_e32 v135, v137
	v_permlane16_swap_b32_e32 v138, v140
	v_permlane16_swap_b32_e32 v139, v141
	global_store_dwordx4 v[144:145], v[134:137], off
	global_store_dwordx4 v[144:145], v[138:141], off offset:256
	v_add_u32_e32 v132, s9, v178
	v_mad_i64_i32 v[132:133], s[62:63], s94, v132, 0
	v_lshl_add_u64 v[132:133], v[132:133], 1, v[130:131]
	v_lshl_add_u64 v[144:145], v[132:133], 0, v[142:143]
	v_cvt_pk_bf16_f32 v134, v78, v79
	v_cvt_pk_bf16_f32 v135, v80, v81
	v_cvt_pk_bf16_f32 v136, v74, v75
	v_cvt_pk_bf16_f32 v137, v76, v77
	v_cvt_pk_bf16_f32 v138, v70, v71
	v_cvt_pk_bf16_f32 v139, v72, v73
	v_cvt_pk_bf16_f32 v140, v66, v67
	v_cvt_pk_bf16_f32 v141, v68, v69
	s_nop 1
	v_permlane16_swap_b32_e32 v134, v136
	v_permlane16_swap_b32_e32 v135, v137
	v_permlane16_swap_b32_e32 v138, v140
	v_permlane16_swap_b32_e32 v139, v141
	global_store_dwordx4 v[144:145], v[134:137], off
	global_store_dwordx4 v[144:145], v[138:141], off offset:256
	v_add_u32_e32 v132, s9, v179
	v_mad_i64_i32 v[132:133], s[62:63], s94, v132, 0
	v_lshl_add_u64 v[132:133], v[132:133], 1, v[130:131]
	v_lshl_add_u64 v[144:145], v[132:133], 0, v[142:143]
	v_cvt_pk_bf16_f32 v134, v62, v63
	v_cvt_pk_bf16_f32 v135, v64, v65
	v_cvt_pk_bf16_f32 v136, v58, v59
	v_cvt_pk_bf16_f32 v137, v60, v61
	v_cvt_pk_bf16_f32 v138, v54, v55
	v_cvt_pk_bf16_f32 v139, v56, v57
	v_cvt_pk_bf16_f32 v140, v50, v51
	v_cvt_pk_bf16_f32 v141, v52, v53
	s_nop 1
	v_permlane16_swap_b32_e32 v134, v136
	v_permlane16_swap_b32_e32 v135, v137
	v_permlane16_swap_b32_e32 v138, v140
	v_permlane16_swap_b32_e32 v139, v141
	global_store_dwordx4 v[144:145], v[134:137], off
	global_store_dwordx4 v[144:145], v[138:141], off offset:256
	v_add_u32_e32 v132, s9, v180
	v_mad_i64_i32 v[132:133], s[62:63], s94, v132, 0
	v_lshl_add_u64 v[132:133], v[132:133], 1, v[130:131]
	v_lshl_add_u64 v[144:145], v[132:133], 0, v[142:143]
	v_cvt_pk_bf16_f32 v134, v46, v47
	v_cvt_pk_bf16_f32 v135, v48, v49
	v_cvt_pk_bf16_f32 v136, v42, v43
	v_cvt_pk_bf16_f32 v137, v44, v45
	v_cvt_pk_bf16_f32 v138, v38, v39
	v_cvt_pk_bf16_f32 v139, v40, v41
	v_cvt_pk_bf16_f32 v140, v34, v35
	v_cvt_pk_bf16_f32 v141, v36, v37
	s_nop 1
	v_permlane16_swap_b32_e32 v134, v136
	v_permlane16_swap_b32_e32 v135, v137
	v_permlane16_swap_b32_e32 v138, v140
	v_permlane16_swap_b32_e32 v139, v141
	global_store_dwordx4 v[144:145], v[134:137], off
	global_store_dwordx4 v[144:145], v[138:141], off offset:256
	v_add_u32_e32 v132, s9, v181
	v_mad_i64_i32 v[132:133], s[62:63], s94, v132, 0
	v_lshl_add_u64 v[132:133], v[132:133], 1, v[130:131]
	v_lshl_add_u64 v[144:145], v[132:133], 0, v[142:143]
	v_cvt_pk_bf16_f32 v134, v30, v31
	v_cvt_pk_bf16_f32 v135, v32, v33
	v_cvt_pk_bf16_f32 v136, v26, v27
	v_cvt_pk_bf16_f32 v137, v28, v29
	v_cvt_pk_bf16_f32 v138, v22, v23
	v_cvt_pk_bf16_f32 v139, v24, v25
	v_cvt_pk_bf16_f32 v140, v18, v19
	v_cvt_pk_bf16_f32 v141, v20, v21
	s_nop 1
	v_permlane16_swap_b32_e32 v134, v136
	v_permlane16_swap_b32_e32 v135, v137
	v_permlane16_swap_b32_e32 v138, v140
	v_permlane16_swap_b32_e32 v139, v141
	global_store_dwordx4 v[144:145], v[134:137], off
	global_store_dwordx4 v[144:145], v[138:141], off offset:256
	v_add_u32_e32 v132, s9, v182
	v_mad_i64_i32 v[132:133], s[62:63], s94, v132, 0
	v_lshl_add_u64 v[130:131], v[132:133], 1, v[130:131]
	v_lshl_add_u64 v[144:145], v[130:131], 0, v[142:143]
	v_cvt_pk_bf16_f32 v134, v14, v15
	v_cvt_pk_bf16_f32 v135, v16, v17
	v_cvt_pk_bf16_f32 v136, v10, v11
	v_cvt_pk_bf16_f32 v137, v12, v13
	v_cvt_pk_bf16_f32 v138, v6, v7
	v_cvt_pk_bf16_f32 v139, v8, v9
	v_cvt_pk_bf16_f32 v140, v2, v3
	v_cvt_pk_bf16_f32 v141, v4, v5
	s_nop 1
	v_permlane16_swap_b32_e32 v134, v136
	v_permlane16_swap_b32_e32 v135, v137
	v_permlane16_swap_b32_e32 v138, v140
	v_permlane16_swap_b32_e32 v139, v141
	global_store_dwordx4 v[144:145], v[134:137], off
	global_store_dwordx4 v[144:145], v[138:141], off offset:256
